# MoE unit descriptors: 31-step LDS compare/add-with-carry chains replaced by one vector compare + scalar popcount (4 phases x 8 units), stacked on previous
# baseline (speedup 1.0000x reference)
.LBB0_665:
	s_or_b64 exec, exec, s[8:9]
	v_lshl_add_u32 v1, v0, 2, 0
	v_add_u32_e32 v1, 0x22000, v1
	v_mov_b32_e32 v3, 0
	v_or_b32_e32 v2, 0x400, v0
	s_mov_b64 s[8:9], -1
	ds_write2st64_b32 v1, v3, v3 offset1:8
	s_and_saveexec_b64 s[10:11], s[8:9]
	v_lshl_add_u32 v1, v2, 2, 0
	v_add_u32_e32 v1, 0x22000, v1
	ds_write_b32 v1, v3
	s_or_b64 exec, exec, s[10:11]
	s_and_saveexec_b64 s[10:11], s[8:9]
	s_add_i32 s2, 0, 0x22000
	v_lshl_add_u32 v1, v2, 2, s2
	v_mov_b32_e32 v2, 0
	ds_write_b32 v1, v2 offset:2048
	s_or_b64 exec, exec, s[10:11]
	v_mov_b32_e32 v1, 0
	s_waitcnt lgkmcnt(0)
	s_barrier
	ds_read_b32 v1, v1 offset:36992
	v_and_b32_e32 v61, 63, v0
	v_lshlrev_b32_e32 v62, 2, v61
	ds_read_b32 v60, v62 offset:36864
	v_add_u32_e32 v61, -1, v61
	v_cmp_gt_u32_e32 vcc, 31, v61
	v_mov_b32_e32 v61, 0x7fffffff
	s_waitcnt lgkmcnt(0)
	s_nop 0
	v_cndmask_b32_e32 v60, v61, v60, vcc
	s_mov_b32 s14, 0
	s_waitcnt lgkmcnt(0)
	v_readfirstlane_b32 s2, v1
	s_ashr_i32 s3, s2, 31
	s_lshr_b32 s3, s3, 24
	s_add_i32 s2, s2, s3
	s_ashr_i32 s17, s2, 8
	s_mul_i32 s17, s17, 6
	s_ashr_i32 s2, s17, 31
	s_lshr_b32 s2, s2, 29
	s_add_i32 s2, s17, s2
	s_ashr_i32 s13, s2, 3
	s_and_b32 s2, s2, -8
	s_sub_i32 s15, s17, s2
	s_add_i32 s12, s13, 1
	s_cmp_ge_i32 s93, s17
	s_cbranch_scc0 .LBB0_671
	s_mov_b64 s[10:11], 0
	s_and_b64 s[8:9], s[6:7], exec
	s_branch .LBB0_672

.LBB0_682:
	s_ashr_i32 s2, s2, 3
	s_add_i32 s3, s10, s2
	s_mul_hi_i32 s2, s3, 0x2aaaaaab
	s_lshr_b32 s8, s2, 31
	s_add_i32 s2, s2, s8
	s_lshl_b32 s8, s2, 8
	v_cmp_ge_i32_e32 vcc, s8, v60
	s_bcnt1_i32_b64 s9, vcc
	v_mov_b32_e32 v1, s9
	s_mul_i32 s8, s2, 6
	s_sub_i32 s3, s3, s8
	v_mul_lo_u32 v1, v1, 6
	s_lshl_b32 s8, s3, 12
	v_add_u32_sdwa v1, v1, s3 dst_sel:WORD_1 dst_unused:UNUSED_PAD src0_sel:DWORD src1_sel:DWORD
	s_nop 0
	v_or_b32_e32 v1, s8, v1
	v_or_b32_e32 v1, s2, v1
	s_mov_b64 s[8:9], s[6:7]
	v_readfirstlane_b32 s14, v1
	s_and_saveexec_b64 s[10:11], s[8:9]
	s_cbranch_execnz .LBB0_676

.LBB0_688:
	s_add_i32 s2, s18, s3
	s_mul_hi_i32 s3, s2, 0x2aaaaaab
	s_lshr_b32 s10, s3, 31
	s_add_i32 s3, s3, s10
	s_lshl_b32 s10, s3, 8
	v_cmp_ge_i32_e32 vcc, s10, v60
	s_bcnt1_i32_b64 s11, vcc
	v_mov_b32_e32 v1, s11
	s_mul_i32 s10, s3, 6
	s_sub_i32 s2, s2, s10
	v_mul_lo_u32 v1, v1, 6
	s_lshl_b32 s10, s2, 12
	v_add_u32_sdwa v1, v1, s2 dst_sel:WORD_1 dst_unused:UNUSED_PAD src0_sel:DWORD src1_sel:DWORD
	s_nop 0
	v_or_b32_e32 v1, s10, v1
	v_or_b32_e32 v1, s3, v1
	s_nop 0
	v_readfirstlane_b32 s2, v1
	s_and_saveexec_b64 s[10:11], s[0:1]
	s_xor_b64 s[10:11], exec, s[10:11]
	s_andn2_saveexec_b64 s[10:11], s[10:11]
	s_or_b64 s[8:9], s[8:9], exec
	s_or_b64 exec, exec, s[10:11]
	s_mov_b32 s20, 2
	s_and_saveexec_b64 s[10:11], s[8:9]

.LBB0_700:
	s_add_i32 s3, s19, s10
	s_mul_hi_i32 s10, s3, 0x2aaaaaab
	s_lshr_b32 s11, s10, 31
	s_add_i32 s18, s10, s11
	s_lshl_b32 s10, s18, 8
	v_cmp_ge_i32_e32 vcc, s10, v60
	s_bcnt1_i32_b64 s11, vcc
	v_mov_b32_e32 v1, s11
	s_mul_i32 s10, s18, 6
	s_sub_i32 s3, s3, s10
	v_mul_lo_u32 v1, v1, 6
	s_lshl_b32 s10, s3, 12
	v_add_u32_sdwa v1, v1, s3 dst_sel:WORD_1 dst_unused:UNUSED_PAD src0_sel:DWORD src1_sel:DWORD
	s_nop 0
	v_or_b32_e32 v1, s10, v1
	v_or_b32_e32 v1, s18, v1
	s_nop 0
	v_readfirstlane_b32 s3, v1
	s_and_saveexec_b64 s[10:11], s[0:1]
	s_xor_b64 s[10:11], exec, s[10:11]
	s_andn2_saveexec_b64 s[10:11], s[10:11]
	s_or_b64 s[8:9], s[8:9], exec
	s_or_b64 exec, exec, s[10:11]
	s_mov_b32 s20, 3
	s_and_saveexec_b64 s[10:11], s[8:9]

.LBB0_712:
	s_add_i32 s10, s20, s10
	s_mul_hi_i32 s11, s10, 0x2aaaaaab
	s_lshr_b32 s18, s11, 31
	s_add_i32 s19, s11, s18
	s_lshl_b32 s11, s19, 8
	v_cmp_ge_i32_e32 vcc, s11, v60
	s_bcnt1_i32_b64 s18, vcc
	v_mov_b32_e32 v1, s18
	s_mul_i32 s11, s19, 6
	s_sub_i32 s10, s10, s11
	v_mul_lo_u32 v1, v1, 6
	s_lshl_b32 s11, s10, 12
	v_add_u32_sdwa v1, v1, s10 dst_sel:WORD_1 dst_unused:UNUSED_PAD src0_sel:DWORD src1_sel:DWORD
	s_nop 0
	v_or_b32_e32 v1, s11, v1
	v_or_b32_e32 v1, s19, v1
	s_nop 0
	v_readfirstlane_b32 s18, v1
	s_and_saveexec_b64 s[10:11], s[0:1]
	s_xor_b64 s[10:11], exec, s[10:11]
	s_andn2_saveexec_b64 s[10:11], s[10:11]
	s_or_b64 s[8:9], s[8:9], exec
	s_or_b64 exec, exec, s[10:11]
	s_mov_b32 s20, 4
	s_and_saveexec_b64 s[10:11], s[8:9]

.LBB0_724:
	s_add_i32 s10, s21, s10
	s_mul_hi_i32 s11, s10, 0x2aaaaaab
	s_lshr_b32 s19, s11, 31
	s_add_i32 s21, s11, s19
	s_lshl_b32 s11, s21, 8
	v_cmp_ge_i32_e32 vcc, s11, v60
	s_bcnt1_i32_b64 s19, vcc
	v_mov_b32_e32 v1, s19
	s_mul_i32 s11, s21, 6
	s_sub_i32 s10, s10, s11
	v_mul_lo_u32 v1, v1, 6
	s_lshl_b32 s11, s10, 12
	v_add_u32_sdwa v1, v1, s10 dst_sel:WORD_1 dst_unused:UNUSED_PAD src0_sel:DWORD src1_sel:DWORD
	s_nop 0
	v_or_b32_e32 v1, s11, v1
	v_or_b32_e32 v1, s21, v1
	s_nop 0
	v_readfirstlane_b32 s19, v1
	s_and_saveexec_b64 s[10:11], s[0:1]
	s_xor_b64 s[10:11], exec, s[10:11]
	s_andn2_saveexec_b64 s[10:11], s[10:11]
	s_or_b64 s[8:9], s[8:9], exec
	s_or_b64 exec, exec, s[10:11]
	s_mov_b32 s20, 5
	s_and_saveexec_b64 s[10:11], s[8:9]

.LBB0_736:
	s_add_i32 s10, s21, s10
	s_mul_hi_i32 s11, s10, 0x2aaaaaab
	s_lshr_b32 s20, s11, 31
	s_add_i32 s22, s11, s20
	s_lshl_b32 s11, s22, 8
	v_cmp_ge_i32_e32 vcc, s11, v60
	s_bcnt1_i32_b64 s20, vcc
	v_mov_b32_e32 v1, s20
	s_mul_i32 s11, s22, 6
	s_sub_i32 s10, s10, s11
	v_mul_lo_u32 v1, v1, 6
	s_lshl_b32 s11, s10, 12
	v_add_u32_sdwa v1, v1, s10 dst_sel:WORD_1 dst_unused:UNUSED_PAD src0_sel:DWORD src1_sel:DWORD
	s_nop 0
	v_or_b32_e32 v1, s11, v1
	v_or_b32_e32 v1, s22, v1
	s_nop 0
	v_readfirstlane_b32 s21, v1
	s_and_saveexec_b64 s[10:11], s[0:1]
	s_xor_b64 s[10:11], exec, s[10:11]
	s_andn2_saveexec_b64 s[10:11], s[10:11]
	s_or_b64 s[8:9], s[8:9], exec
	s_or_b64 exec, exec, s[10:11]
	s_mov_b32 s20, 6
	s_and_saveexec_b64 s[10:11], s[8:9]

.LBB0_748:
	s_add_i32 s11, s22, s10
	s_mul_hi_i32 s10, s11, 0x2aaaaaab
	s_lshr_b32 s20, s10, 31
	s_add_i32 s10, s10, s20
	s_lshl_b32 s20, s10, 8
	v_cmp_ge_i32_e32 vcc, s20, v60
	s_bcnt1_i32_b64 s22, vcc
	v_mov_b32_e32 v1, s22
	s_mul_i32 s20, s10, 6
	s_sub_i32 s11, s11, s20
	v_mul_lo_u32 v1, v1, 6
	s_lshl_b32 s20, s11, 12
	v_add_u32_sdwa v1, v1, s11 dst_sel:WORD_1 dst_unused:UNUSED_PAD src0_sel:DWORD src1_sel:DWORD
	s_nop 0
	v_or_b32_e32 v1, s20, v1
	v_or_b32_e32 v1, s10, v1
	s_nop 0
	v_readfirstlane_b32 s22, v1
	s_and_saveexec_b64 s[24:25], s[0:1]
	s_xor_b64 s[0:1], exec, s[24:25]
	s_andn2_saveexec_b64 s[0:1], s[0:1]
	s_or_b64 s[8:9], s[8:9], exec
	s_or_b64 exec, exec, s[0:1]
	s_mov_b32 s20, 7
	s_and_saveexec_b64 s[0:1], s[8:9]

.LBB0_760:
	s_add_i32 s0, s10, s0
	s_mul_hi_i32 s1, s0, 0x2aaaaaab
	s_lshr_b32 s8, s1, 31
	s_add_i32 s8, s1, s8
	s_lshl_b32 s1, s8, 8
	s_mov_b32 s20, 8
	v_cmp_ge_i32_e32 vcc, s1, v60
	s_bcnt1_i32_b64 s9, vcc
	v_mov_b32_e32 v1, s9
	s_mul_i32 s1, s8, 6
	s_sub_i32 s0, s0, s1
	v_mul_lo_u32 v1, v1, 6
	s_lshl_b32 s1, s0, 12
	v_add_u32_sdwa v1, v1, s0 dst_sel:WORD_1 dst_unused:UNUSED_PAD src0_sel:DWORD src1_sel:DWORD
	s_nop 0
	v_or_b32_e32 v1, s1, v1
	v_or_b32_e32 v1, s8, v1
	s_nop 0
	v_readfirstlane_b32 s23, v1
	s_and_saveexec_b64 s[0:1], s[6:7]

.LBB0_870:
	s_or_b64 exec, exec, s[6:7]
	s_add_i32 s0, 0, 0x27d80
	v_mov_b32_e32 v1, s0
	s_waitcnt vmcnt(0) lgkmcnt(0)
	s_barrier
	ds_read_b32 v1, v1
	v_and_b32_e32 v61, 63, v0
	v_lshlrev_b32_e32 v62, 2, v61
	v_add_u32_e32 v62, 0x27d00, v62
	ds_read_b32 v60, v62
	v_add_u32_e32 v61, -1, v61
	v_cmp_gt_u32_e32 vcc, 31, v61
	v_mov_b32_e32 v61, 0x7fffffff
	s_waitcnt lgkmcnt(0)
	s_nop 0
	v_cndmask_b32_e32 v60, v61, v60, vcc
	s_mov_b32 s2, 0
	s_mov_b32 s23, 0
	s_waitcnt lgkmcnt(0)
	v_readfirstlane_b32 s0, v1
	s_ashr_i32 s1, s0, 31
	s_lshr_b32 s1, s1, 24
	s_add_i32 s0, s0, s1
	s_ashr_i32 s1, s0, 8
	s_lshl_b32 s6, s1, 3
	s_cmp_ge_i32 s93, s6
	s_mov_b32 s0, 0
	s_cbranch_scc1 .LBB0_872
	s_ashr_i32 s0, s93, 31
	s_lshr_b32 s0, s0, 29
	s_add_i32 s0, s93, s0
	s_ashr_i32 s3, s0, 3
	s_and_b32 s0, s0, -8
	s_sub_i32 s0, s93, s0
	s_lshr_b32 s7, s0, 31
	s_add_i32 s7, s1, s7
	s_mul_i32 s0, s7, s0
	s_add_i32 s0, s0, s3
	s_ashr_i32 s3, s0, 31
	s_lshr_b32 s3, s3, 29
	s_add_i32 s3, s0, s3
	s_ashr_i32 s7, s3, 3
	s_lshl_b32 s8, s7, 8
	s_and_b32 s3, s3, -8
	s_sub_i32 s0, s0, s3
	s_lshl_b32 s3, s0, 12
	s_lshl_b32 s0, s0, 16
	s_mov_b32 s23, 1
	v_cmp_ge_i32_e32 vcc, s8, v60
	s_bcnt1_i32_b64 s9, vcc
	v_mov_b32_e32 v1, s9
	v_lshlrev_b32_e32 v1, 19, v1
	v_add_u32_e32 v1, s0, v1
	v_or_b32_e32 v1, s3, v1
	v_or_b32_e32 v1, s7, v1
	s_nop 0
	v_readfirstlane_b32 s0, v1
.LBB0_872:
	s_add_i32 s3, s80, s93
	s_cmp_ge_i32 s3, s6
	s_cbranch_scc1 .LBB0_874
	s_ashr_i32 s2, s3, 31
	s_lshr_b32 s2, s2, 29
	s_add_i32 s2, s3, s2
	s_ashr_i32 s7, s2, 3
	s_and_b32 s2, s2, -8
	s_sub_i32 s2, s3, s2
	s_lshr_b32 s3, s2, 31
	s_add_i32 s3, s1, s3
	s_mul_i32 s2, s3, s2
	s_add_i32 s2, s2, s7
	s_ashr_i32 s3, s2, 31
	s_lshr_b32 s3, s3, 29
	s_add_i32 s3, s2, s3
	s_ashr_i32 s7, s3, 3
	s_lshl_b32 s8, s7, 8
	s_and_b32 s3, s3, -8
	s_sub_i32 s2, s2, s3
	s_lshl_b32 s3, s2, 12
	s_lshl_b32 s2, s2, 16
	s_mov_b32 s23, 2
	v_cmp_ge_i32_e32 vcc, s8, v60
	s_bcnt1_i32_b64 s9, vcc
	v_mov_b32_e32 v1, s9
	v_lshlrev_b32_e32 v1, 19, v1
	v_add_u32_e32 v1, s2, v1
	v_or_b32_e32 v1, s3, v1
	v_or_b32_e32 v1, s7, v1
	s_nop 0
	v_readfirstlane_b32 s2, v1
.LBB0_874:
	s_lshl_b32 s7, s80, 1
	s_add_i32 s7, s7, s93
	s_mov_b32 s3, 0
	s_cmp_ge_i32 s7, s6
	s_mov_b32 s20, 0
	s_cbranch_scc1 .LBB0_876
	s_ashr_i32 s8, s7, 31
	s_lshr_b32 s8, s8, 29
	s_add_i32 s8, s7, s8
	s_ashr_i32 s9, s8, 3
	s_and_b32 s8, s8, -8
	s_sub_i32 s7, s7, s8
	s_lshr_b32 s8, s7, 31
	s_add_i32 s8, s1, s8
	s_mul_i32 s7, s8, s7
	s_add_i32 s7, s7, s9
	s_ashr_i32 s8, s7, 31
	s_lshr_b32 s8, s8, 29
	s_add_i32 s8, s7, s8
	s_ashr_i32 s9, s8, 3
	s_lshl_b32 s10, s9, 8
	s_and_b32 s8, s8, -8
	s_sub_i32 s7, s7, s8
	s_lshl_b32 s8, s7, 12
	s_lshl_b32 s7, s7, 16
	s_mov_b32 s23, 3
	v_cmp_ge_i32_e32 vcc, s10, v60
	s_bcnt1_i32_b64 s11, vcc
	v_mov_b32_e32 v1, s11
	v_lshlrev_b32_e32 v1, 19, v1
	v_add_u32_e32 v1, s7, v1
	v_or_b32_e32 v1, s8, v1
	v_or_b32_e32 v1, s9, v1
	s_nop 0
	v_readfirstlane_b32 s20, v1
.LBB0_876:
	s_add_i32 s7, s88, s93
	s_cmp_ge_i32 s7, s6
	s_cbranch_scc1 .LBB0_878
	s_ashr_i32 s3, s7, 31
	s_lshr_b32 s3, s3, 29
	s_add_i32 s3, s7, s3
	s_ashr_i32 s8, s3, 3
	s_and_b32 s3, s3, -8
	s_sub_i32 s3, s7, s3
	s_lshr_b32 s7, s3, 31
	s_add_i32 s7, s1, s7
	s_mul_i32 s3, s7, s3
	s_add_i32 s3, s3, s8
	s_ashr_i32 s7, s3, 31
	s_lshr_b32 s7, s7, 29
	s_add_i32 s7, s3, s7
	s_ashr_i32 s8, s7, 3
	s_lshl_b32 s9, s8, 8
	s_and_b32 s7, s7, -8
	s_sub_i32 s3, s3, s7
	s_lshl_b32 s7, s3, 12
	s_lshl_b32 s3, s3, 16
	s_mov_b32 s23, 4
	v_cmp_ge_i32_e32 vcc, s9, v60
	s_bcnt1_i32_b64 s10, vcc
	v_mov_b32_e32 v1, s10
	v_lshlrev_b32_e32 v1, 19, v1
	v_add_u32_e32 v1, s3, v1
	v_or_b32_e32 v1, s7, v1
	v_or_b32_e32 v1, s8, v1
	s_nop 0
	v_readfirstlane_b32 s3, v1
.LBB0_878:
	s_lshl_b32 s7, s80, 2
	s_add_i32 s7, s7, s93
	s_mov_b32 s21, 0
	s_cmp_ge_i32 s7, s6
	s_mov_b32 s22, 0
	s_cbranch_scc1 .LBB0_880
	s_ashr_i32 s8, s7, 31
	s_lshr_b32 s8, s8, 29
	s_add_i32 s8, s7, s8
	s_ashr_i32 s9, s8, 3
	s_and_b32 s8, s8, -8
	s_sub_i32 s7, s7, s8
	s_lshr_b32 s8, s7, 31
	s_add_i32 s8, s1, s8
	s_mul_i32 s7, s8, s7
	s_add_i32 s7, s7, s9
	s_ashr_i32 s8, s7, 31
	s_lshr_b32 s8, s8, 29
	s_add_i32 s8, s7, s8
	s_ashr_i32 s9, s8, 3
	s_lshl_b32 s10, s9, 8
	s_and_b32 s8, s8, -8
	s_sub_i32 s7, s7, s8
	s_lshl_b32 s8, s7, 12
	s_lshl_b32 s7, s7, 16
	s_mov_b32 s23, 5
	v_cmp_ge_i32_e32 vcc, s10, v60
	s_bcnt1_i32_b64 s11, vcc
	v_mov_b32_e32 v1, s11
	v_lshlrev_b32_e32 v1, 19, v1
	v_add_u32_e32 v1, s7, v1
	v_or_b32_e32 v1, s8, v1
	v_or_b32_e32 v1, s9, v1
	s_nop 0
	v_readfirstlane_b32 s22, v1
.LBB0_880:
	s_add_i32 s7, s87, s93
	s_cmp_ge_i32 s7, s6
	s_cbranch_scc1 .LBB0_882
	s_ashr_i32 s8, s7, 31
	s_lshr_b32 s8, s8, 29
	s_add_i32 s8, s7, s8
	s_ashr_i32 s9, s8, 3
	s_and_b32 s8, s8, -8
	s_sub_i32 s7, s7, s8
	s_lshr_b32 s8, s7, 31
	s_add_i32 s8, s1, s8
	s_mul_i32 s7, s8, s7
	s_add_i32 s7, s7, s9
	s_ashr_i32 s8, s7, 31
	s_lshr_b32 s8, s8, 29
	s_add_i32 s8, s7, s8
	s_ashr_i32 s9, s8, 3
	s_lshl_b32 s10, s9, 8
	s_and_b32 s8, s8, -8
	s_sub_i32 s7, s7, s8
	s_lshl_b32 s8, s7, 12
	s_lshl_b32 s7, s7, 16
	s_mov_b32 s23, 6
	v_cmp_ge_i32_e32 vcc, s10, v60
	s_bcnt1_i32_b64 s11, vcc
	v_mov_b32_e32 v1, s11
	v_lshlrev_b32_e32 v1, 19, v1
	v_add_u32_e32 v1, s7, v1
	v_or_b32_e32 v1, s8, v1
	v_or_b32_e32 v1, s9, v1
	s_nop 0
	v_readfirstlane_b32 s21, v1
.LBB0_882:
	s_add_i32 s7, s86, s93
	s_mov_b32 s24, 0
	s_cmp_ge_i32 s7, s6
	s_mov_b32 s25, 0
	s_cbranch_scc1 .LBB0_884
	s_ashr_i32 s8, s7, 31
	s_lshr_b32 s8, s8, 29
	s_add_i32 s8, s7, s8
	s_ashr_i32 s9, s8, 3
	s_and_b32 s8, s8, -8
	s_sub_i32 s7, s7, s8
	s_lshr_b32 s8, s7, 31
	s_add_i32 s8, s1, s8
	s_mul_i32 s7, s8, s7
	s_add_i32 s7, s7, s9
	s_ashr_i32 s8, s7, 31
	s_lshr_b32 s8, s8, 29
	s_add_i32 s8, s7, s8
	s_ashr_i32 s9, s8, 3
	s_lshl_b32 s10, s9, 8
	s_and_b32 s8, s8, -8
	s_sub_i32 s7, s7, s8
	s_lshl_b32 s8, s7, 12
	s_lshl_b32 s7, s7, 16
	s_mov_b32 s23, 7
	v_cmp_ge_i32_e32 vcc, s10, v60
	s_bcnt1_i32_b64 s11, vcc
	v_mov_b32_e32 v1, s11
	v_lshlrev_b32_e32 v1, 19, v1
	v_add_u32_e32 v1, s7, v1
	v_or_b32_e32 v1, s8, v1
	v_or_b32_e32 v1, s9, v1
	s_nop 0
	v_readfirstlane_b32 s25, v1
.LBB0_884:
	s_add_i32 s7, s89, s93
	s_cmp_ge_i32 s7, s6
	s_cbranch_scc1 .LBB0_886
	s_ashr_i32 s6, s7, 31
	s_lshr_b32 s6, s6, 29
	s_add_i32 s6, s7, s6
	s_ashr_i32 s8, s6, 3
	s_and_b32 s6, s6, -8
	s_sub_i32 s6, s7, s6
	s_lshr_b32 s7, s6, 31
	s_add_i32 s1, s1, s7
	s_mul_i32 s1, s1, s6
	s_add_i32 s1, s1, s8
	s_ashr_i32 s6, s1, 31
	s_lshr_b32 s6, s6, 29
	s_add_i32 s6, s1, s6
	s_ashr_i32 s7, s6, 3
	s_lshl_b32 s8, s7, 8
	s_and_b32 s6, s6, -8
	s_sub_i32 s1, s1, s6
	s_lshl_b32 s6, s1, 12
	s_lshl_b32 s1, s1, 16
	s_mov_b32 s23, 8
	v_cmp_ge_i32_e32 vcc, s8, v60
	s_bcnt1_i32_b64 s9, vcc
	v_mov_b32_e32 v1, s9
	v_lshlrev_b32_e32 v1, 19, v1
	v_add_u32_e32 v1, s1, v1
	v_or_b32_e32 v1, s6, v1
	v_or_b32_e32 v1, s7, v1
	s_nop 0
	v_readfirstlane_b32 s24, v1

.LBB0_1376:
	s_or_b64 exec, exec, s[8:9]
	v_lshl_add_u32 v1, v0, 2, 0
	v_add_u32_e32 v1, 0x22000, v1
	v_mov_b32_e32 v2, 0
	ds_write2st64_b32 v1, v2, v2 offset1:8
	v_or_b32_e32 v1, 0x400, v0
	s_mov_b64 s[8:9], -1
	s_and_saveexec_b64 s[10:11], s[8:9]
	v_lshl_add_u32 v3, v1, 2, 0
	v_add_u32_e32 v3, 0x22000, v3
	ds_write_b32 v3, v2
	s_or_b64 exec, exec, s[10:11]
	s_and_saveexec_b64 s[10:11], s[8:9]
	s_add_i32 s2, 0, 0x22000
	v_lshl_add_u32 v1, v1, 2, s2
	v_mov_b32_e32 v2, 0
	ds_write_b32 v1, v2 offset:2048
	s_or_b64 exec, exec, s[10:11]
	v_mov_b32_e32 v1, 0
	s_waitcnt lgkmcnt(0)
	s_barrier
	ds_read_b32 v1, v1 offset:36992
	v_and_b32_e32 v61, 63, v0
	v_lshlrev_b32_e32 v62, 2, v61
	ds_read_b32 v60, v62 offset:36864
	v_add_u32_e32 v61, -1, v61
	v_cmp_gt_u32_e32 vcc, 31, v61
	v_mov_b32_e32 v61, 0x7fffffff
	s_waitcnt lgkmcnt(0)
	s_nop 0
	v_cndmask_b32_e32 v60, v61, v60, vcc
	s_mov_b32 s14, 0
	s_waitcnt lgkmcnt(0)
	v_readfirstlane_b32 s2, v1
	s_ashr_i32 s3, s2, 31
	s_lshr_b32 s3, s3, 24
	s_add_i32 s2, s2, s3
	s_ashr_i32 s17, s2, 8
	s_mul_i32 s17, s17, 6
	s_ashr_i32 s2, s17, 31
	s_lshr_b32 s2, s2, 29
	s_add_i32 s2, s17, s2
	s_ashr_i32 s13, s2, 3
	s_and_b32 s2, s2, -8
	s_sub_i32 s15, s17, s2
	s_add_i32 s12, s13, 1
	s_cmp_ge_i32 s93, s17
	s_cbranch_scc0 .LBB0_1382
	s_mov_b64 s[10:11], 0
	s_and_b64 s[8:9], s[6:7], exec
	s_branch .LBB0_1383

.LBB0_1580:
	s_or_b64 exec, exec, s[0:1]
	s_add_i32 s0, 0, 0x27d80
	v_mov_b32_e32 v2, s0
	s_waitcnt vmcnt(0) lgkmcnt(0)
	s_barrier
	ds_read_b32 v2, v2
	v_and_b32_e32 v61, 63, v0
	v_lshlrev_b32_e32 v62, 2, v61
	v_add_u32_e32 v62, 0x27d00, v62
	ds_read_b32 v60, v62
	v_add_u32_e32 v61, -1, v61
	v_cmp_gt_u32_e32 vcc, 31, v61
	v_mov_b32_e32 v61, 0x7fffffff
	s_waitcnt lgkmcnt(0)
	s_nop 0
	v_cndmask_b32_e32 v60, v61, v60, vcc
	s_mov_b32 s2, 0
	s_mov_b32 s33, 0
	s_waitcnt lgkmcnt(0)
	v_readfirstlane_b32 s0, v2
	s_ashr_i32 s1, s0, 31
	s_lshr_b32 s1, s1, 24
	s_add_i32 s0, s0, s1
	s_ashr_i32 s1, s0, 8
	s_lshl_b32 s6, s1, 3
	s_cmp_ge_i32 s93, s6
	s_mov_b32 s0, 0
	s_cbranch_scc1 .LBB0_1582
	s_ashr_i32 s0, s93, 31
	s_lshr_b32 s0, s0, 29
	s_add_i32 s0, s93, s0
	s_ashr_i32 s3, s0, 3
	s_and_b32 s0, s0, -8
	s_sub_i32 s0, s93, s0
	s_lshr_b32 s7, s0, 31
	s_add_i32 s7, s1, s7
	s_mul_i32 s0, s7, s0
	s_add_i32 s0, s0, s3
	s_ashr_i32 s3, s0, 31
	s_lshr_b32 s3, s3, 29
	s_add_i32 s3, s0, s3
	s_ashr_i32 s7, s3, 3
	s_lshl_b32 s8, s7, 8
	s_and_b32 s3, s3, -8
	s_sub_i32 s0, s0, s3
	s_lshl_b32 s3, s0, 12
	s_lshl_b32 s0, s0, 16
	s_mov_b32 s33, 1
	v_cmp_ge_i32_e32 vcc, s8, v60
	s_bcnt1_i32_b64 s9, vcc
	v_mov_b32_e32 v2, s9
	v_lshlrev_b32_e32 v2, 19, v2
	v_add_u32_e32 v2, s0, v2
	v_or_b32_e32 v2, s3, v2
	v_or_b32_e32 v2, s7, v2
	s_nop 0
	v_readfirstlane_b32 s0, v2
.LBB0_1582:
	s_add_i32 s3, s80, s93
	s_cmp_ge_i32 s3, s6
	s_cbranch_scc1 .LBB0_1584
	s_ashr_i32 s2, s3, 31
	s_lshr_b32 s2, s2, 29
	s_add_i32 s2, s3, s2
	s_ashr_i32 s7, s2, 3
	s_and_b32 s2, s2, -8
	s_sub_i32 s2, s3, s2
	s_lshr_b32 s3, s2, 31
	s_add_i32 s3, s1, s3
	s_mul_i32 s2, s3, s2
	s_add_i32 s2, s2, s7
	s_ashr_i32 s3, s2, 31
	s_lshr_b32 s3, s3, 29
	s_add_i32 s3, s2, s3
	s_ashr_i32 s7, s3, 3
	s_lshl_b32 s8, s7, 8
	s_and_b32 s3, s3, -8
	s_sub_i32 s2, s2, s3
	s_lshl_b32 s3, s2, 12
	s_lshl_b32 s2, s2, 16
	s_mov_b32 s33, 2
	v_cmp_ge_i32_e32 vcc, s8, v60
	s_bcnt1_i32_b64 s9, vcc
	v_mov_b32_e32 v2, s9
	v_lshlrev_b32_e32 v2, 19, v2
	v_add_u32_e32 v2, s2, v2
	v_or_b32_e32 v2, s3, v2
	v_or_b32_e32 v2, s7, v2
	s_nop 0
	v_readfirstlane_b32 s2, v2
.LBB0_1584:
	s_lshl_b32 s7, s80, 1
	s_add_i32 s7, s7, s93
	s_mov_b32 s3, 0
	s_cmp_ge_i32 s7, s6
	s_mov_b32 s24, 0
	s_cbranch_scc1 .LBB0_1586
	s_ashr_i32 s8, s7, 31
	s_lshr_b32 s8, s8, 29
	s_add_i32 s8, s7, s8
	s_ashr_i32 s9, s8, 3
	s_and_b32 s8, s8, -8
	s_sub_i32 s7, s7, s8
	s_lshr_b32 s8, s7, 31
	s_add_i32 s8, s1, s8
	s_mul_i32 s7, s8, s7
	s_add_i32 s7, s7, s9
	s_ashr_i32 s8, s7, 31
	s_lshr_b32 s8, s8, 29
	s_add_i32 s8, s7, s8
	s_ashr_i32 s9, s8, 3
	s_lshl_b32 s10, s9, 8
	s_and_b32 s8, s8, -8
	s_sub_i32 s7, s7, s8
	s_lshl_b32 s8, s7, 12
	s_lshl_b32 s7, s7, 16
	s_mov_b32 s33, 3
	v_cmp_ge_i32_e32 vcc, s10, v60
	s_bcnt1_i32_b64 s11, vcc
	v_mov_b32_e32 v2, s11
	v_lshlrev_b32_e32 v2, 19, v2
	v_add_u32_e32 v2, s7, v2
	v_or_b32_e32 v2, s8, v2
	v_or_b32_e32 v2, s9, v2
	s_nop 0
	v_readfirstlane_b32 s24, v2
.LBB0_1586:
	s_add_i32 s7, s88, s93
	s_cmp_ge_i32 s7, s6
	s_cbranch_scc1 .LBB0_1588
	s_ashr_i32 s3, s7, 31
	s_lshr_b32 s3, s3, 29
	s_add_i32 s3, s7, s3
	s_ashr_i32 s8, s3, 3
	s_and_b32 s3, s3, -8
	s_sub_i32 s3, s7, s3
	s_lshr_b32 s7, s3, 31
	s_add_i32 s7, s1, s7
	s_mul_i32 s3, s7, s3
	s_add_i32 s3, s3, s8
	s_ashr_i32 s7, s3, 31
	s_lshr_b32 s7, s7, 29
	s_add_i32 s7, s3, s7
	s_ashr_i32 s8, s7, 3
	s_lshl_b32 s9, s8, 8
	s_and_b32 s7, s7, -8
	s_sub_i32 s3, s3, s7
	s_lshl_b32 s7, s3, 12
	s_lshl_b32 s3, s3, 16
	s_mov_b32 s33, 4
	v_cmp_ge_i32_e32 vcc, s9, v60
	s_bcnt1_i32_b64 s10, vcc
	v_mov_b32_e32 v2, s10
	v_lshlrev_b32_e32 v2, 19, v2
	v_add_u32_e32 v2, s3, v2
	v_or_b32_e32 v2, s7, v2
	v_or_b32_e32 v2, s8, v2
	s_nop 0
	v_readfirstlane_b32 s3, v2
.LBB0_1588:
	s_lshl_b32 s7, s80, 2
	s_add_i32 s7, s7, s93
	s_mov_b32 s25, 0
	s_cmp_ge_i32 s7, s6
	s_mov_b32 s26, 0
	s_cbranch_scc1 .LBB0_1590
	s_ashr_i32 s8, s7, 31
	s_lshr_b32 s8, s8, 29
	s_add_i32 s8, s7, s8
	s_ashr_i32 s9, s8, 3
	s_and_b32 s8, s8, -8
	s_sub_i32 s7, s7, s8
	s_lshr_b32 s8, s7, 31
	s_add_i32 s8, s1, s8
	s_mul_i32 s7, s8, s7
	s_add_i32 s7, s7, s9
	s_ashr_i32 s8, s7, 31
	s_lshr_b32 s8, s8, 29
	s_add_i32 s8, s7, s8
	s_ashr_i32 s9, s8, 3
	s_lshl_b32 s10, s9, 8
	s_and_b32 s8, s8, -8
	s_sub_i32 s7, s7, s8
	s_lshl_b32 s8, s7, 12
	s_lshl_b32 s7, s7, 16
	s_mov_b32 s33, 5
	v_cmp_ge_i32_e32 vcc, s10, v60
	s_bcnt1_i32_b64 s11, vcc
	v_mov_b32_e32 v2, s11
	v_lshlrev_b32_e32 v2, 19, v2
	v_add_u32_e32 v2, s7, v2
	v_or_b32_e32 v2, s8, v2
	v_or_b32_e32 v2, s9, v2
	s_nop 0
	v_readfirstlane_b32 s26, v2
.LBB0_1590:
	s_add_i32 s7, s87, s93
	s_cmp_ge_i32 s7, s6
	s_cbranch_scc1 .LBB0_1592
	s_ashr_i32 s8, s7, 31
	s_lshr_b32 s8, s8, 29
	s_add_i32 s8, s7, s8
	s_ashr_i32 s9, s8, 3
	s_and_b32 s8, s8, -8
	s_sub_i32 s7, s7, s8
	s_lshr_b32 s8, s7, 31
	s_add_i32 s8, s1, s8
	s_mul_i32 s7, s8, s7
	s_add_i32 s7, s7, s9
	s_ashr_i32 s8, s7, 31
	s_lshr_b32 s8, s8, 29
	s_add_i32 s8, s7, s8
	s_ashr_i32 s9, s8, 3
	s_lshl_b32 s10, s9, 8
	s_and_b32 s8, s8, -8
	s_sub_i32 s7, s7, s8
	s_lshl_b32 s8, s7, 12
	s_lshl_b32 s7, s7, 16
	s_mov_b32 s33, 6
	v_cmp_ge_i32_e32 vcc, s10, v60
	s_bcnt1_i32_b64 s11, vcc
	v_mov_b32_e32 v2, s11
	v_lshlrev_b32_e32 v2, 19, v2
	v_add_u32_e32 v2, s7, v2
	v_or_b32_e32 v2, s8, v2
	v_or_b32_e32 v2, s9, v2
	s_nop 0
	v_readfirstlane_b32 s25, v2
.LBB0_1592:
	s_add_i32 s7, s86, s93
	s_mov_b32 s34, 0
	s_cmp_ge_i32 s7, s6
	s_mov_b32 s35, 0
	s_cbranch_scc1 .LBB0_1594
	s_ashr_i32 s8, s7, 31
	s_lshr_b32 s8, s8, 29
	s_add_i32 s8, s7, s8
	s_ashr_i32 s9, s8, 3
	s_and_b32 s8, s8, -8
	s_sub_i32 s7, s7, s8
	s_lshr_b32 s8, s7, 31
	s_add_i32 s8, s1, s8
	s_mul_i32 s7, s8, s7
	s_add_i32 s7, s7, s9
	s_ashr_i32 s8, s7, 31
	s_lshr_b32 s8, s8, 29
	s_add_i32 s8, s7, s8
	s_ashr_i32 s9, s8, 3
	s_lshl_b32 s10, s9, 8
	s_and_b32 s8, s8, -8
	s_sub_i32 s7, s7, s8
	s_lshl_b32 s8, s7, 12
	s_lshl_b32 s7, s7, 16
	s_mov_b32 s33, 7
	v_cmp_ge_i32_e32 vcc, s10, v60
	s_bcnt1_i32_b64 s11, vcc
	v_mov_b32_e32 v2, s11
	v_lshlrev_b32_e32 v2, 19, v2
	v_add_u32_e32 v2, s7, v2
	v_or_b32_e32 v2, s8, v2
	v_or_b32_e32 v2, s9, v2
	s_nop 0
	v_readfirstlane_b32 s35, v2
.LBB0_1594:
	s_add_i32 s7, s89, s93
	s_cmp_ge_i32 s7, s6
	s_cbranch_scc1 .LBB0_1596
	s_ashr_i32 s6, s7, 31
	s_lshr_b32 s6, s6, 29
	s_add_i32 s6, s7, s6
	s_ashr_i32 s8, s6, 3
	s_and_b32 s6, s6, -8
	s_sub_i32 s6, s7, s6
	s_lshr_b32 s7, s6, 31
	s_add_i32 s1, s1, s7
	s_mul_i32 s1, s1, s6
	s_add_i32 s1, s1, s8
	s_ashr_i32 s6, s1, 31
	s_lshr_b32 s6, s6, 29
	s_add_i32 s6, s1, s6
	s_ashr_i32 s7, s6, 3
	s_lshl_b32 s8, s7, 8
	s_and_b32 s6, s6, -8
	s_sub_i32 s1, s1, s6
	s_lshl_b32 s6, s1, 12
	s_lshl_b32 s1, s1, 16
	s_mov_b32 s33, 8
	v_cmp_ge_i32_e32 vcc, s8, v60
	s_bcnt1_i32_b64 s9, vcc
	v_mov_b32_e32 v2, s9
	v_lshlrev_b32_e32 v2, 19, v2
	v_add_u32_e32 v2, s1, v2
	v_or_b32_e32 v2, s6, v2
	v_or_b32_e32 v2, s7, v2
	s_nop 0
	v_readfirstlane_b32 s34, v2
